# speedup vs baseline: 1.0274x; 1.0077x over previous
.LBB1_8:
	s_or_b64 exec, exec, s[4:5]
	v_cmp_gt_u32_e64 s[10:11], 35, v0
	v_mov_b32_e32 v214, 0
	v_lshlrev_b32_e32 v215, 2, v0
	s_and_saveexec_b64 s[8:9], s[10:11]
	global_load_dword v214, v215, s[6:7]
	s_or_b64 exec, exec, s[8:9]
	s_load_dwordx2 s[4:5], s[0:1], 0x38
	s_movk_i32 s0, 0x23f
	v_mul_i32_i24_e32 v125, 0xffffffdd, v129
	v_mul_i32_i24_e32 v131, 0xffffffdd, v130
	v_cmp_lt_u32_e64 s[0:1], s0, v0
	v_lshlrev_b32_e32 v126, 4, v0
	s_and_saveexec_b64 s[8:9], s[0:1]
	s_xor_b64 s[0:1], exec, s[8:9]
	v_lshlrev_b32_e32 v114, 4, v0
	v_or_b32_e32 v121, 0xfffffe00, v0
	s_andn2_saveexec_b64 s[8:9], s[0:1]
	s_cbranch_execz .LBB1_14
	v_or_b32_e32 v121, 0xfffffe00, v0
	v_mov_b32_e32 v114, 0
	v_add_u32_e32 v127, 0, v126
	s_mov_b64 s[10:11], 0
	v_mov_b32_e32 v115, v114
	v_mov_b32_e32 v116, v114
	v_mov_b32_e32 v117, v114
	v_mov_b32_e32 v148, v121

.LBB1_15:
	v_add_u32_e32 v149, 0x200, v149
	v_cmp_lt_u32_e64 s[0:1], s3, v149
	ds_write_b128 v148, v[114:117]
	s_or_b64 s[8:9], s[0:1], s[8:9]
	v_add_u32_e32 v148, 0x2000, v148
	s_andn2_b64 exec, exec, s[8:9]
	s_cbranch_execnz .LBB1_15
	s_or_b64 exec, exec, s[8:9]
	v_add_u32_e32 v116, 0x2400, v127
	v_mov_b32_e32 v127, 0
	s_waitcnt lgkmcnt(0)
	global_load_dwordx4 v[190:193], v126, s[4:5]
	s_add_u32 s4, s4, 0x2000
	s_addc_u32 s5, s5, 0
	global_load_dwordx4 v[194:197], v126, s[4:5]
	s_add_u32 s4, s4, 0x2000
	s_addc_u32 s5, s5, 0
	global_load_dwordx4 v[198:201], v126, s[4:5]
	s_add_u32 s4, s4, 0x2000
	s_addc_u32 s5, s5, 0
	global_load_dwordx4 v[202:205], v126, s[4:5]
	s_add_u32 s4, s4, 0x2000
	s_addc_u32 s5, s5, 0
	global_load_dwordx4 v[206:209], v126, s[4:5]
	s_add_u32 s4, s4, 0x2000
	s_addc_u32 s5, s5, 0
	s_movk_i32 s3, 0x1d0
	v_cmp_gt_u32_e64 s[0:1], s3, v0
	s_and_saveexec_b64 s[8:9], s[0:1]
	global_load_dwordx4 v[210:213], v126, s[4:5]
	s_or_b64 exec, exec, s[8:9]
	s_waitcnt vmcnt(5)
	ds_write_b128 v116, v[190:193]
	s_waitcnt vmcnt(4)
	ds_write_b128 v116, v[194:197] offset:8192
	s_waitcnt vmcnt(3)
	ds_write_b128 v116, v[198:201] offset:16384
	s_waitcnt vmcnt(2)
	ds_write_b128 v116, v[202:205] offset:24576
	s_waitcnt vmcnt(1)
	ds_write_b128 v116, v[206:209] offset:32768
	s_waitcnt vmcnt(0)
	s_and_saveexec_b64 s[8:9], s[0:1]
	ds_write_b128 v116, v[210:213] offset:40960
	s_or_b64 exec, exec, s[8:9]
	v_cmp_gt_u32_e64 s[0:1], 48, v0
	s_waitcnt lgkmcnt(0)
	s_barrier
	s_and_saveexec_b64 s[4:5], s[0:1]
	s_cbranch_execz .LBB1_22
	v_lshl_add_u32 v115, v0, 2, 0
	s_waitcnt vmcnt(0)
	ds_write_b32 v115, v214 offset:57600

_Z11attn_kernelPKtS0_PKfS2_S2_PfS3_:
	s_load_dwordx4 s[12:15], s[0:1], 0x8
	v_lshlrev_b32_e32 v1, 4, v0
	v_or_b32_e32 v10, 0x4000, v1
	v_or_b32_e32 v18, 0x8000, v1
	v_or_b32_e32 v19, 0xc000, v1
	v_or_b32_e32 v30, 0x10000, v1
	v_or_b32_e32 v38, 0x1c000, v1
	s_movk_i32 s3, 0x380
	v_cmp_gt_u32_e32 vcc, s3, v0
	s_waitcnt lgkmcnt(0)
	s_and_saveexec_b64 s[4:5], vcc
	s_cbranch_execz .Lattn_s8
	global_load_dwordx4 v[34:37], v38, s[12:13]
.Lattn_s8:
	s_or_b64 exec, exec, s[4:5]
	global_load_dwordx4 v[2:5], v1, s[12:13]
	global_load_dwordx4 v[6:9], v10, s[12:13]
	s_nop 0
	global_load_dwordx4 v[10:13], v18, s[12:13]
	global_load_dwordx4 v[14:17], v19, s[12:13]
	v_or_b32_e32 v31, 0x14000, v1
	global_load_dwordx4 v[18:21], v30, s[12:13]
	global_load_dwordx4 v[22:25], v31, s[12:13]
	v_or_b32_e32 v32, 0x1800, v0
	v_lshlrev_b32_e32 v33, 4, v32
	global_load_dwordx4 v[26:29], v33, s[12:13]
	v_add_u32_e32 v1, 0, v1
	v_add_u32_e32 v30, 0, v30
	v_add_u32_e32 v31, 0, v31
	v_add_u32_e32 v33, 0, v33
	s_waitcnt vmcnt(6)
	ds_write_b128 v1, v[2:5]
	s_waitcnt vmcnt(5)
	ds_write_b128 v1, v[6:9] offset:16384
	s_waitcnt vmcnt(4)
	ds_write_b128 v1, v[10:13] offset:32768
	s_waitcnt vmcnt(3)
	ds_write_b128 v1, v[14:17] offset:49152
	s_waitcnt vmcnt(2)
	ds_write_b128 v30, v[18:21]
	s_waitcnt vmcnt(1)
	ds_write_b128 v31, v[22:25]
	s_waitcnt vmcnt(0)
	ds_write_b128 v33, v[26:29]
	s_and_saveexec_b64 s[4:5], vcc
	ds_write_b128 v38, v[34:37]
	s_or_b64 exec, exec, s[4:5]
	s_load_dwordx2 s[12:13], s[0:1], 0x0
	s_load_dwordx8 s[4:11], s[0:1], 0x18
	v_and_b32_e32 v108, 15, v0
	v_bfe_u32 v1, v0, 4, 5
	v_mul_u32_u24_e32 v3, 0x2d0, v1
	v_lshlrev_b32_e32 v4, 1, v108
	v_add3_u32 v3, v3, v4, 0
	v_or_b32_e32 v2, -16, v108
	v_add_u32_e32 v4, 0x17600, v3
	v_mov_b32_e32 v3, 0
	s_mov_b64 s[0:1], 0
	s_movk_i32 s3, 0x14f
	s_waitcnt lgkmcnt(0)
	s_barrier
	ds_read_u16 v72, v4
	ds_read_u16 v73, v4 offset:32
	ds_read_u16 v74, v4 offset:64
	ds_read_u16 v75, v4 offset:96
	ds_read_u16 v76, v4 offset:128
	ds_read_u16 v77, v4 offset:160
	ds_read_u16 v78, v4 offset:192
	ds_read_u16 v79, v4 offset:224
	ds_read_u16 v80, v4 offset:256
	ds_read_u16 v81, v4 offset:288
	ds_read_u16 v82, v4 offset:320
	ds_read_u16 v83, v4 offset:352
	ds_read_u16 v84, v4 offset:384
	ds_read_u16 v85, v4 offset:416
	ds_read_u16 v86, v4 offset:448
	ds_read_u16 v87, v4 offset:480
	ds_read_u16 v88, v4 offset:512
	ds_read_u16 v89, v4 offset:544
	ds_read_u16 v90, v4 offset:576
	ds_read_u16 v91, v4 offset:608
	ds_read_u16 v92, v4 offset:640
	ds_read_u16 v93, v4 offset:672
	s_waitcnt lgkmcnt(11)
	v_lshlrev_b32_e32 v72, 16, v72
	v_max_f32_e32 v72, v72, v72
	v_max_f32_e32 v72, 0, v72
	v_add_f32_e32 v3, v3, v72
	v_lshlrev_b32_e32 v73, 16, v73
	v_max_f32_e32 v73, v73, v73
	v_max_f32_e32 v73, 0, v73
	v_add_f32_e32 v3, v3, v73
	v_lshlrev_b32_e32 v74, 16, v74
	v_max_f32_e32 v74, v74, v74
	v_max_f32_e32 v74, 0, v74
	v_add_f32_e32 v3, v3, v74
	v_lshlrev_b32_e32 v75, 16, v75
	v_max_f32_e32 v75, v75, v75
	v_max_f32_e32 v75, 0, v75
	v_add_f32_e32 v3, v3, v75
	v_lshlrev_b32_e32 v76, 16, v76
	v_max_f32_e32 v76, v76, v76
	v_max_f32_e32 v76, 0, v76
	v_add_f32_e32 v3, v3, v76
	v_lshlrev_b32_e32 v77, 16, v77
	v_max_f32_e32 v77, v77, v77
	v_max_f32_e32 v77, 0, v77
	v_add_f32_e32 v3, v3, v77
	v_lshlrev_b32_e32 v78, 16, v78
	v_max_f32_e32 v78, v78, v78
	v_max_f32_e32 v78, 0, v78
	v_add_f32_e32 v3, v3, v78
	v_lshlrev_b32_e32 v79, 16, v79
	v_max_f32_e32 v79, v79, v79
	v_max_f32_e32 v79, 0, v79
	v_add_f32_e32 v3, v3, v79
	v_lshlrev_b32_e32 v80, 16, v80
	v_max_f32_e32 v80, v80, v80
	v_max_f32_e32 v80, 0, v80
	v_add_f32_e32 v3, v3, v80
	v_lshlrev_b32_e32 v81, 16, v81
	v_max_f32_e32 v81, v81, v81
	v_max_f32_e32 v81, 0, v81
	v_add_f32_e32 v3, v3, v81
	v_lshlrev_b32_e32 v82, 16, v82
	v_max_f32_e32 v82, v82, v82
	v_max_f32_e32 v82, 0, v82
	v_add_f32_e32 v3, v3, v82
	s_waitcnt lgkmcnt(0)
	v_lshlrev_b32_e32 v83, 16, v83
	v_max_f32_e32 v83, v83, v83
	v_max_f32_e32 v83, 0, v83
	v_add_f32_e32 v3, v3, v83
	v_lshlrev_b32_e32 v84, 16, v84
	v_max_f32_e32 v84, v84, v84
	v_max_f32_e32 v84, 0, v84
	v_add_f32_e32 v3, v3, v84
	v_lshlrev_b32_e32 v85, 16, v85
	v_max_f32_e32 v85, v85, v85
	v_max_f32_e32 v85, 0, v85
	v_add_f32_e32 v3, v3, v85
	v_lshlrev_b32_e32 v86, 16, v86
	v_max_f32_e32 v86, v86, v86
	v_max_f32_e32 v86, 0, v86
	v_add_f32_e32 v3, v3, v86
	v_lshlrev_b32_e32 v87, 16, v87
	v_max_f32_e32 v87, v87, v87
	v_max_f32_e32 v87, 0, v87
	v_add_f32_e32 v3, v3, v87
	v_lshlrev_b32_e32 v88, 16, v88
	v_max_f32_e32 v88, v88, v88
	v_max_f32_e32 v88, 0, v88
	v_add_f32_e32 v3, v3, v88
	v_lshlrev_b32_e32 v89, 16, v89
	v_max_f32_e32 v89, v89, v89
	v_max_f32_e32 v89, 0, v89
	v_add_f32_e32 v3, v3, v89
	v_lshlrev_b32_e32 v90, 16, v90
	v_max_f32_e32 v90, v90, v90
	v_max_f32_e32 v90, 0, v90
	v_add_f32_e32 v3, v3, v90
	v_lshlrev_b32_e32 v91, 16, v91
	v_max_f32_e32 v91, v91, v91
	v_max_f32_e32 v91, 0, v91
	v_add_f32_e32 v3, v3, v91
	v_lshlrev_b32_e32 v92, 16, v92
	v_max_f32_e32 v92, v92, v92
	v_max_f32_e32 v92, 0, v92
	v_add_f32_e32 v3, v3, v92
	v_lshlrev_b32_e32 v93, 16, v93
	v_max_f32_e32 v93, v93, v93
	v_max_f32_e32 v93, 0, v93
	v_add_f32_e32 v3, v3, v93
	s_or_b64 exec, exec, s[0:1]
	v_add_f32_dpp v2, v3, v3 quad_perm:[1,0,3,2] row_mask:0xf bank_mask:0xf bound_ctrl:1
	v_cmp_eq_u32_e32 vcc, 0, v108
	s_nop 0
	v_add_f32_dpp v2, v2, v2 quad_perm:[2,3,0,1] row_mask:0xf bank_mask:0xf bound_ctrl:1
	s_nop 1
	v_add_f32_dpp v2, v2, v2 row_half_mirror row_mask:0xf bank_mask:0xf bound_ctrl:1
	s_nop 1
	v_mov_b32_dpp v3, v2 row_mirror row_mask:0xf bank_mask:0xf bound_ctrl:1
	s_and_saveexec_b64 s[0:1], vcc
	s_cbranch_execz .LBB2_6
	v_add_f32_e32 v2, v2, v3
	v_mov_b32_e32 v3, 0x3c23d70a
	v_lshl_add_u32 v1, v1, 2, 0
	v_fmac_f32_e32 v3, 0x3f804189, v2
	v_add_u32_e32 v1, 0x1f780, v1
	v_xor_b32_e32 v2, 0x80000000, v3
	ds_write_b32 v1, v2
